# band tile loop: next-tile K/V prefetch uses 5 running 64-bit addresses (uniform per-tile increment) instead of recomputing row*pitch each tile; on top of h0/mod batching
# speedup vs baseline: 1.0030x; 1.0030x over previous
.LBB0_1258:
	s_and_b32 s1, s37, 15
	s_ashr_i32 s50, s37, 4
	s_bfe_u32 s47, s37, 0x20002
	s_or_b32 s48, s1, s29
	s_cmp_lg_u32 s50, 3
	s_mov_b32 s0, s37
	s_cselect_b64 s[54:55], -1, 0
	s_add_i32 s37, s37, 8
	s_and_b32 s49, s37, 15
	s_ashr_i32 s60, s37, 4
	s_bfe_u32 s51, s37, 0x20002
	s_or_b32 s52, s49, s29
	s_cmp_eq_u32 s60, 2
	s_cselect_b32 s49, s49, 0
	s_cselect_b32 s52, s93, s52
	s_cselect_b32 s53, 4, 0
	s_cmp_eq_u32 s50, 2
	s_cselect_b32 s1, s1, 0
	s_cselect_b32 s48, s93, s48
	s_cselect_b32 s56, 4, 0
	s_cmp_eq_u32 s60, 1
	s_cselect_b32 s61, s51, s49
	s_cselect_b32 s3, s31, s52
	s_cselect_b32 s73, 2, s53
	s_cmp_eq_u32 s50, 1
	s_cselect_b32 s1, s47, s1
	s_cselect_b32 s79, s31, s48
	s_cselect_b32 s47, 2, s56
	s_or_b32 s56, s38, s1
	s_cmp_lt_i32 s0, 56
	s_cselect_b64 s[52:53], -1, 0
	s_cmp_gt_i32 s0, 55
	s_cselect_b64 s[48:49], -1, 0
	s_sub_i32 s0, 4, s79
	s_max_i32 s51, s0, 0
	s_cmp_eq_u32 s50, 3
	s_cselect_b64 s[58:59], -1, 0
	s_and_b64 s[0:1], s[58:59], exec
	s_movk_i32 s23, 0x1000
	s_cselect_b32 s0, s23, 0x400
	s_movk_i32 s82, 0x1100
	s_cselect_b32 s18, s95, s94
	s_cselect_b32 s19, s82, 0x800
	s_add_u32 s20, s12, s0
	s_addc_u32 s21, s13, 0
	s_cmp_eq_u32 s60, 3
	s_cselect_b64 s[0:1], -1, 0
	s_and_b64 s[0:1], s[0:1], exec
	s_cselect_b32 s66, 0xc00, 0
	s_cselect_b32 s0, s23, 0x400
	s_cselect_b32 s82, s82, 0x800
	s_cselect_b32 s83, s95, s94
	s_or_b32 s60, s38, s61
	s_add_u32 vcc_lo, s12, s82
	s_addc_u32 vcc_hi, s13, 0
	s_lshl_b32 s82, s83, 7
	s_add_u32 vcc_lo, vcc_lo, s82
	s_addc_u32 vcc_hi, vcc_hi, 0
	v_mov_b32_e32 v153, v3
	s_lshl_b32 s18, s18, 7
	v_lshl_add_u64 v[20:21], vcc, 0, v[152:153]
	s_add_u32 vcc_lo, s20, s18
	s_addc_u32 vcc_hi, s21, 0
	s_add_u32 s19, s12, s19
	s_addc_u32 s20, s13, 0
	v_lshl_add_u64 v[156:157], vcc, 0, v[154:155]
	s_add_u32 vcc_lo, s19, s18
	s_addc_u32 vcc_hi, s20, 0
	s_lshl_b32 s3, s3, 5
	v_or_b32_e32 v2, s3, v182
	s_mov_b32 s61, s39
	v_lshlrev_b64 v[22:23], s73, v[2:3]
	v_lshl_add_u64 v[22:23], v[22:23], 0, s[60:61]
	v_mov_b64_e32 v[24:25], s[12:13]
	v_lshl_add_u64 v[158:159], vcc, 0, v[152:153]
	v_mad_u64_u32 v[24:25], vcc, v22, s5, v[24:25]
	v_mad_i32_i24 v25, v23, s5, v25
	v_lshl_add_u64 v[22:23], v[24:25], 0, s[66:67]
	s_mov_b32 s1, s67
	v_lshl_add_u64 v[22:23], v[22:23], 0, s[42:43]
	s_mov_b32 s83, s67
	v_lshl_add_u64 v[160:161], v[22:23], 0, v[154:155]
	v_lshl_add_u64 v[22:23], v[24:25], 0, s[0:1]
	v_lshl_add_u64 v[22:23], v[22:23], 0, s[82:83]
	v_or_b32_e32 v2, s3, v1
	v_lshl_add_u64 v[162:163], v[22:23], 0, v[154:155]
	v_lshlrev_b64 v[22:23], s73, v[2:3]
	v_lshl_add_u64 v[22:23], v[22:23], 0, s[60:61]
	v_mad_u64_u32 v[164:165], s[0:1], v22, s5, v[20:21]
	v_or_b32_e32 v2, s3, v183
	v_mad_i32_i24 v165, v23, s5, v165
	v_lshlrev_b64 v[22:23], s73, v[2:3]
	v_lshl_add_u64 v[22:23], v[22:23], 0, s[60:61]
	v_mad_u64_u32 v[166:167], s[0:1], v22, s5, v[20:21]
	v_or_b32_e32 v2, s3, v184
	v_mad_i32_i24 v167, v23, s5, v167
	v_lshlrev_b64 v[22:23], s73, v[2:3]
	v_lshl_add_u64 v[22:23], v[22:23], 0, s[60:61]
	v_mad_u64_u32 v[168:169], s[0:1], v22, s5, v[20:21]
	v_or_b32_e32 v2, s3, v185
	v_mad_i32_i24 v169, v23, s5, v169
	v_lshlrev_b64 v[22:23], s73, v[2:3]
	v_lshl_add_u64 v[22:23], v[22:23], 0, s[60:61]
	v_mad_u64_u32 v[170:171], s[0:1], v22, s5, v[20:21]
	s_lshl_b32 s0, s79, 5
	s_nop 0
	v_or_b32_e32 v2, s0, v1
	v_add_u32_e32 v172, s0, v186
	v_add_u32_e32 v174, s0, v187
	v_add_u32_e32 v176, s0, v188
	v_lshl_add_u64 v[178:179], v[2:3], 0, s[96:97]
	v_or_b32_e32 v2, s0, v182
	s_mul_i32 s0, s50, 0x1880
	v_mov_b32_e32 v194, 0
	v_mov_b64_e32 v[52:53], v[96:97]
	v_mov_b64_e32 v[56:57], v[92:93]
	v_mov_b64_e32 v[60:61], v[88:89]
	v_mov_b64_e32 v[64:65], v[84:85]
	s_mov_b32 s41, 4
	s_mov_b32 s57, s39
	v_mad_i32_i24 v171, v23, s5, v171
	v_ashrrev_i32_e32 v173, 31, v172
	v_ashrrev_i32_e32 v175, 31, v174
	v_ashrrev_i32_e32 v177, 31, v176
	v_lshl_add_u64 v[180:181], v[2:3], 0, s[96:97]
	v_add_u32_e32 v153, s0, v193
	v_mov_b32_e32 v196, 0xf149f2ca
	v_mov_b64_e32 v[54:55], v[98:99]
	v_mov_b64_e32 v[58:59], v[94:95]
	v_mov_b64_e32 v[62:63], v[90:91]
	v_mov_b64_e32 v[66:67], v[86:87]
	v_mov_b32_e32 v20, 0
	v_mov_b32_e32 v21, v194
	v_mov_b32_e32 v22, v194
	v_mov_b32_e32 v23, v194
	v_mov_b32_e32 v24, v194
	v_mov_b32_e32 v25, v194
	v_mov_b32_e32 v26, v194
	v_mov_b32_e32 v27, v194
	v_mov_b32_e32 v28, v194
	v_mov_b32_e32 v29, v194
	v_mov_b32_e32 v30, v194
	v_mov_b32_e32 v31, v194
	v_mov_b32_e32 v32, v194
	v_mov_b32_e32 v33, v194
	v_mov_b32_e32 v34, v194
	v_mov_b32_e32 v35, v194
	v_mov_b32_e32 v36, 0
	v_mov_b32_e32 v37, v194
	v_mov_b32_e32 v38, v194
	v_mov_b32_e32 v39, v194
	v_mov_b32_e32 v40, v194
	v_mov_b32_e32 v41, v194
	v_mov_b32_e32 v42, v194
	v_mov_b32_e32 v43, v194
	v_mov_b32_e32 v44, v194
	v_mov_b32_e32 v45, v194
	v_mov_b32_e32 v46, v194
	v_mov_b32_e32 v47, v194
	v_mov_b32_e32 v48, v194
	v_mov_b32_e32 v49, v194
	v_mov_b32_e32 v50, v194
	v_mov_b32_e32 v51, v194
	v_mov_b32_e32 v205, 0
	v_lshlrev_b32_e32 v204, s47, v180
	v_add_u32_e32 v204, s56, v204
	v_mul_u32_u24_e32 v204, s5, v204
	v_lshl_add_u64 v[180:181], v[204:205], 0, v[156:157]
	v_lshlrev_b32_e32 v204, s47, v178
	v_add_u32_e32 v204, s56, v204
	v_mul_u32_u24_e32 v204, s5, v204
	v_lshl_add_u64 v[178:179], v[204:205], 0, v[158:159]
	v_lshlrev_b32_e32 v204, s47, v176
	v_add_u32_e32 v204, s56, v204
	v_mul_u32_u24_e32 v204, s5, v204
	v_lshl_add_u64 v[176:177], v[204:205], 0, v[158:159]
	v_lshlrev_b32_e32 v204, s47, v174
	v_add_u32_e32 v204, s56, v204
	v_mul_u32_u24_e32 v204, s5, v204
	v_lshl_add_u64 v[174:175], v[204:205], 0, v[158:159]
	v_lshlrev_b32_e32 v204, s47, v172
	v_add_u32_e32 v204, s56, v204
	v_mul_u32_u24_e32 v204, s5, v204
	v_lshl_add_u64 v[172:173], v[204:205], 0, v[158:159]
	v_mov_b32_e32 v206, 32
	v_lshlrev_b32_e32 v206, s47, v206
	v_mul_u32_u24_e32 v206, s5, v206
	v_sub_u32_e32 v206, 0, v206
	v_mov_b32_e32 v207, -1

.LBB0_1265:
	s_waitcnt vmcnt(0)
	v_mfma_f32_32x32x16_bf16 v[52:67], v[144:147], v[124:127], 0
	ds_write_b128 v191, v[128:131] offset:32768
	ds_write_b128 v191, v[120:123] offset:33280
	ds_write_b128 v191, v[104:107] offset:33792
	ds_write_b128 v191, v[100:103] offset:34304
	ds_read2_b32 v[198:199], v153 offset0:26 offset1:27
	s_andn2_b64 vcc, exec, s[82:83]
	v_mfma_f32_32x32x16_bf16 v[52:67], v[140:143], v[116:119], v[52:67]
	v_mfma_f32_32x32x16_bf16 v[52:67], v[136:139], v[112:115], v[52:67]
	v_mfma_f32_32x32x16_bf16 v[52:67], v[132:135], v[108:111], v[52:67]
	s_cbranch_vccnz .Lband_nopf
	global_load_dwordx4 v[144:147], v[180:181], off
	global_load_dwordx4 v[140:143], v[180:181], off offset:32
	global_load_dwordx4 v[136:139], v[180:181], off offset:64
	global_load_dwordx4 v[132:135], v[180:181], off offset:96
	global_load_dwordx4 v[128:131], v[178:179], off
	global_load_dwordx4 v[120:123], v[176:177], off
	global_load_dwordx4 v[104:107], v[174:175], off
	global_load_dwordx4 v[100:103], v[172:173], off

.LBB0_1267:
	v_add_f32_e32 v197, v57, v58
	v_fmac_f32_e32 v197, v194, v56
	s_add_i32 s41, s41, -1
	v_lshl_add_u64 v[172:173], v[172:173], 0, v[206:207]
	v_lshl_add_u64 v[174:175], v[174:175], 0, v[206:207]
	v_lshl_add_u64 v[176:177], v[176:177], 0, v[206:207]
	v_lshl_add_u64 v[178:179], v[178:179], 0, v[206:207]
	v_lshl_add_u64 v[180:181], v[180:181], 0, v[206:207]
	v_add_u32_e32 v153, 0x80, v153
	s_and_b64 vcc, exec, s[60:61]
	s_cbranch_vccnz .LBB0_1269
	v_mov_b32_e32 v196, v195
	v_mov_b32_e32 v194, v197
	s_branch .LBB0_1259
